# v9 with 128 converter workgroups
# baseline (speedup 1.0000x reference)
.LBB0_226:
	s_cmp_lt_i32 s28, 3
	s_cselect_b64 s[0:1], -1, 0
	s_cmp_gt_i32 s29, 2
	s_cselect_b64 s[6:7], -1, 0
	s_and_b64 s[0:1], s[0:1], s[6:7]
	s_andn2_b64 vcc, exec, s[0:1]
	s_cbranch_vccnz .LBB0_398
	s_cmpk_lg_i32 s33, 0x100
	s_cselect_b32 s3, s33, 0x80
	s_sub_i32 s6, s33, s3
	s_cmp_lt_i32 s2, s6
	s_cselect_b64 s[0:1], -1, 0
	s_sub_i32 s30, s2, s6
	s_cmpk_gt_i32 s30, 0x2fff
	s_cselect_b64 s[6:7], -1, 0
	s_or_b64 s[0:1], s[0:1], s[6:7]
	v_lshrrev_b32_e32 v82, 5, v0
	v_lshlrev_b32_e32 v80, 4, v0
	v_lshrrev_b32_e32 v1, 7, v0
	v_lshrrev_b32_e32 v81, 3, v0
	s_and_b64 vcc, exec, s[0:1]
	s_cbranch_vccnz .LBB0_237
	v_readlane_b32 s6, v252, 0
	v_readlane_b32 s7, v252, 1
	v_readfirstlane_b32 s34, v0
	s_nop 4
	s_sub_u32 s6, s6, 0xe8
	s_subb_u32 s7, s7, 0
	s_load_dwordx2 s[8:9], s[6:7], 0xa8
	s_load_dwordx2 s[10:11], s[6:7], 0xb8
	s_lshr_b32 s34, s34, 6
	s_add_u32 s12, s26, 0x5800000
	s_addc_u32 s13, s27, 0
	s_add_u32 s14, s26, 0x25800000
	s_addc_u32 s15, s27, 0
	s_mov_b32 s35, 0xc3e00000
	v_mov_b32_e32 v160, 0x43e00000
	s_mov_b32 s31, 128
	s_sub_u32 s0, 0x2fff, s30
	s_mul_hi_u32 s41, s0, 0x2000000
	s_add_u32 s41, s41, 1
	v_and_b32_e32 v77, 63, v0
	v_and_b32_e32 v66, 31, v77
	v_lshlrev_b32_e32 v66, 4, v66
	v_lshrrev_b32_e32 v67, 5, v77
	v_lshlrev_b32_e32 v68, 4, v77
	v_lshl_add_u32 v69, v67, 9, v66
	s_lshr_b32 s0, s34, 1
	v_and_b32_e32 v78, 3, v77
	v_xor_b32_e32 v78, s0, v78
	v_and_b32_e32 v71, 4, v77
	v_or_b32_e32 v78, v78, v71
	v_lshlrev_b32_e32 v78, 4, v78
	s_and_b32 s0, s34, 1
	s_lshl_b32 s0, s0, 3
	v_lshl_or_b32 v71, v77, 9, s0
	v_or_b32_e32 v71, v71, v78
	v_xor_b32_e32 v72, 64, v71
	v_add_u32_e32 v73, 0x8000, v71
	v_add_u32_e32 v74, 0x8000, v72
	s_lshl_b32 s0, s34, 1
	v_add_u32_e32 v78, s0, v67
	v_xor_b32_e32 v78, v78, v77
	v_and_b32_e32 v78, 7, v78
	v_lshlrev_b32_e32 v78, 4, v78
	v_lshrrev_b32_e32 v75, 3, v77
	s_lshl_b32 s0, s34, 3
	v_add_u32_e32 v75, s0, v75
	v_and_b32_e32 v76, 7, v77
	v_lshlrev_b32_e32 v76, 4, v76
	v_lshl_add_u32 v76, v75, 11, v76
	v_lshl_add_u32 v75, v75, 7, v78
	s_waitcnt lgkmcnt(0)
	s_min_u32 s0, s30, 0x2fff
	s_add_u32 s30, s30, s31
	s_cmp_lt_u32 s0, 0x2000
	s_cbranch_scc0 .Lcv_w2_1
	s_lshr_b32 s1, s0, 8
	s_bfe_u32 s3, s0, 0x40004
	s_bfe_u32 s7, s0, 0x30001
	s_and_b32 s0, s0, 1
	s_lshl_b32 s6, s1, 25
	s_lshl_b32 s49, s3, 21
	s_add_u32 s6, s6, s49
	s_lshl_b32 s49, s34, 17
	s_add_u32 s6, s6, s49
	s_lshl_b32 s49, s0, 13
	s_add_u32 s6, s6, s49
	s_lshl_b32 s49, s7, 10
	s_add_u32 s6, s6, s49
	s_add_u32 s62, s8, s6
	s_addc_u32 s63, s9, 0
	s_lshl_b32 s6, s1, 23
	s_lshl_b32 s49, s7, 20
	s_add_u32 s6, s6, s49
	s_lshl_b32 s49, s0, 18
	s_add_u32 s6, s6, s49
	s_lshl_b32 s49, s3, 7
	s_add_u32 s6, s6, s49
	s_add_u32 s52, s12, s6
	s_addc_u32 s53, s13, 0
	s_mov_b32 s70, 0x4000
	s_mov_b32 s71, 0xe4000
	s_mov_b32 s86, 0x60000
	v_mov_b32_e32 v70, v68
	s_branch .Lcv_dec_done_1
